# P16 final combine: hoisted final-norm gain loads out of the row loop, removed per-chunk pointer reload and waits, prefetch next row token record
# speedup vs baseline: 1.0148x; 1.0085x over previous
; #define LAS __attribute__((address_space(3)))
; __device__ __forceinline__ float bf_lo(unsigned w) { return __uint_as_float(w << 16); }
; __device__ __forceinline__ float bf_hi(unsigned w) { return __uint_as_float(w & 0xffff0000u); }
; __device__ __forceinline__ f32x4 ld4_bf(const bf16_t* p) { const u32x2 w = *(const u32x2*)p; return (f32x4){bf_lo(w.x), bf_hi(w.x), bf_lo(w.y), bf_hi(w.y)}; }
; __device__ __forceinline__ float sq4(const f32x4 v) { return (v[0] * v[0] + v[1] * v[1]) + (v[2] * v[2] + v[3] * v[3]); }
; __device__ __forceinline__ void phase_final(const Ctx& P, volatile LAS int* tab, int vcu, int G) {
;     const int tid = threadIdx.x, lane = tid & 63, wave = __builtin_amdgcn_readfirstlane(tid >> 6);
;     const int gw = vcu * 8 + wave, NGW = G * 8;
;     const float* mod = (const float*)(P.ws + WS_MOD) + (size_t)5 * NMOD; const int* tok = (const int*)(P.ws + WS_TOK); const bf16_t* YB = (const bf16_t*)(P.ws + WS_YB);
;     for (int row = gw; row < ML; row += NGW) {
;         const int e1 = tok[row * 8], pos1 = tok[row * 8 + 1], e2 = tok[row * 8 + 2], pos2 = tok[row * 8 + 3]; const float p1 = ((const float*)tok)[row * 8 + 4], p2 = ((const float*)tok)[row * 8 + 5];
;         const bf16_t* y1 = YB + (size_t)(tab[8 + e1] * 256 + pos1) * DM; const bf16_t* y2 = YB + (size_t)(tab[8 + e2] * 256 + pos2) * DM;
;         const bf16_t* xr = (const bf16_t*)(P.ws + WS_XA) + (size_t)row * DM; const float* g2 = mod + (size_t)(row >> 12) * NMOD + 5 * DM;
;         f32x4 v[8]; float ss = 0.f;
; #pragma unroll
;         for (int j = 0; j < 8; ++j) { const int c = 4 * lane + 256 * j; const f32x4 x4 = ld4_bf(xr + c), g4 = *(const f32x4*)(g2 + c); const u32x2 a = *(const u32x2*)(y1 + c), b = *(const u32x2*)(y2 + c);
;             const f32x4 ya = (f32x4){bf_lo(a.x), bf_hi(a.x), bf_lo(a.y), bf_hi(a.y)}, yb = (f32x4){bf_lo(b.x), bf_hi(b.x), bf_lo(b.y), bf_hi(b.y)};
;             v[j] = x4 + g4 * (ya * p1 + yb * p2); ss += sq4(v[j]); }
;         ss = wave_sum(ss); const float rstd = __builtin_amdgcn_rsqf(ss * (1.0f / DM) + EPS);
; #pragma unroll
;         for (int j = 0; j < 8; ++j) { const int c = 4 * lane + 256 * j; const f32x4 fg = *(const f32x4*)(P.in[34] + c); *(f32x4*)(P.out + (size_t)row * DM + c) = v[j] * rstd * fg; }
.LBB0_2710:
	s_or_b64 exec, exec, s[0:1]
	v_readfirstlane_b32 s0, v0
	s_lshr_b32 s1, s0, 6
	s_lshl_b32 s3, s33, 3
	s_add_i32 s10, s1, s3
	s_cmpk_gt_i32 s10, 0x3fff
	s_waitcnt lgkmcnt(0)
	s_barrier
	s_cbranch_scc1 .LBB0_2713
	v_lshlrev_b32_e32 v1, 2, v0
	v_and_b32_e32 v4, 0xfc, v1
	v_mbcnt_lo_u32_b32 v1, -1, 0
	v_mbcnt_hi_u32_b32 v1, -1, v1
	v_and_b32_e32 v5, 64, v1
	v_add_u32_e32 v5, 64, v5
	v_xor_b32_e32 v6, 1, v1
	v_cmp_lt_i32_e32 vcc, v6, v5
	s_lshl_b32 s0, s39, 3
	v_mov_b32_e32 v29, 0
	v_cndmask_b32_e32 v6, v1, v6, vcc
	v_lshlrev_b32_e32 v58, 2, v6
	v_xor_b32_e32 v6, 2, v1
	v_cmp_lt_i32_e32 vcc, v6, v5
	v_lshlrev_b32_e32 v28, 1, v4
	s_add_u32 s11, s36, 0x200000
	v_cndmask_b32_e32 v6, v1, v6, vcc
	v_lshlrev_b32_e32 v59, 2, v6
	v_xor_b32_e32 v6, 4, v1
	v_cmp_lt_i32_e32 vcc, v6, v5
	v_lshl_add_u64 v[20:21], s[36:37], 0, v[28:29]
	s_mov_b64 s[4:5], 0x24ac0000
	v_cndmask_b32_e32 v6, v1, v6, vcc
	v_lshlrev_b32_e32 v60, 2, v6
	v_xor_b32_e32 v6, 8, v1
	v_cmp_lt_i32_e32 vcc, v6, v5
	s_addc_u32 s12, s37, 0
	v_lshl_add_u64 v[30:31], v[20:21], 0, s[4:5]
	v_cndmask_b32_e32 v6, v1, v6, vcc
	v_lshlrev_b32_e32 v61, 2, v6
	v_xor_b32_e32 v6, 16, v1
	v_cmp_lt_i32_e32 vcc, v6, v5
	s_lshl_b32 s2, s33, 6
	s_lshl_b32 s4, s1, 3
	v_cndmask_b32_e32 v6, v1, v6, vcc
	s_add_i32 s2, s2, s4
	s_lshl_b32 s13, s39, 6
	s_ashr_i32 s4, s3, 31
	v_lshlrev_b32_e32 v62, 2, v6
	v_xor_b32_e32 v6, 32, v1
	s_add_u32 s6, s1, s3
	v_cmp_lt_i32_e32 vcc, v6, v5
	s_addc_u32 s7, 0, s4
	s_lshl_b64 s[4:5], s[6:7], 13
	v_cndmask_b32_e32 v1, v1, v6, vcc
	v_and_b32_e32 v5, 63, v0
	v_lshlrev_b32_e32 v63, 2, v1
	v_lshl_or_b32 v0, v5, 4, s4
	v_mov_b32_e32 v1, s5
	s_waitcnt vmcnt(0)
	v_lshl_add_u64 v[0:1], v[2:3], 0, v[0:1]
	s_mov_b64 s[4:5], 0x1000
	s_ashr_i32 s1, s0, 31
	v_lshl_add_u64 v[32:33], v[0:1], 0, s[4:5]
	s_lshl_b64 s[4:5], s[0:1], 13
	s_lshl_b64 s[6:7], s[6:7], 12
	s_add_u32 s6, s36, s6
	v_lshlrev_b32_e32 v28, 3, v5
	s_addc_u32 s7, s37, s7
	v_or_b32_e32 v6, 0x100, v4
	v_or_b32_e32 v8, 0x200, v4
	v_or_b32_e32 v10, 0x300, v4
	v_or_b32_e32 v12, 0x400, v4
	v_or_b32_e32 v14, 0x500, v4
	v_or_b32_e32 v16, 0x600, v4
	v_or_b32_e32 v18, 0x700, v4
	v_lshl_add_u64 v[0:1], s[6:7], 0, v[28:29]
	s_mov_b64 s[6:7], 0x1c2c0800
	v_lshl_add_u64 v[34:35], v[0:1], 0, s[6:7]
	s_lshl_b64 s[6:7], s[0:1], 12
	s_add_i32 s1, 0, 0x20100
	v_lshlrev_b32_e32 v28, 2, v4
	v_lshlrev_b32_e32 v64, 2, v6
	v_lshlrev_b32_e32 v65, 2, v8
	v_lshlrev_b32_e32 v66, 2, v10
	v_lshlrev_b32_e32 v36, 2, v12
	v_mov_b32_e32 v37, v29
	v_lshlrev_b32_e32 v38, 2, v14
	v_mov_b32_e32 v39, v29
	v_lshlrev_b32_e32 v40, 2, v16
	v_mov_b32_e32 v41, v29
	v_lshlrev_b32_e32 v42, 2, v18
	v_mov_b32_e32 v43, v29
	v_mov_b32_e32 v67, 0x358637bd
	v_mov_b64_e32 v[44:45], s[8:9]
	flat_load_dwordx2 v[82:83], v[44:45] offset:272
	s_ashr_i32 s3, s2, 31
	s_lshl_b64 s[8:9], s[2:3], 2
	s_add_u32 s8, s11, s8
	s_addc_u32 s9, s12, s9
	global_load_dwordx4 v[194:197], v29, s[8:9]
	global_load_dwordx2 v[198:199], v29, s[8:9] offset:16
	s_mov_b64 s[14:15], 0x1000
	s_waitcnt vmcnt(2) lgkmcnt(0)
	v_lshl_add_u64 v[82:83], v[82:83], 0, v[28:29]
	v_lshl_add_u64 v[84:85], v[82:83], 0, s[14:15]
	global_load_dwordx4 v[162:165], v[82:83], off
	global_load_dwordx4 v[166:169], v[82:83], off offset:1024
	global_load_dwordx4 v[170:173], v[82:83], off offset:2048
	global_load_dwordx4 v[174:177], v[82:83], off offset:3072
	global_load_dwordx4 v[178:181], v[84:85], off
	global_load_dwordx4 v[182:185], v[84:85], off offset:1024
	global_load_dwordx4 v[186:189], v[84:85], off offset:2048
	global_load_dwordx4 v[190:193], v[84:85], off offset:3072
	s_waitcnt vmcnt(0)
.LBB0_2712:
	v_mov_b32_e32 v16, v194
	v_mov_b32_e32 v17, v195
	v_mov_b32_e32 v18, v196
	v_mov_b32_e32 v19, v197
	v_mov_b32_e32 v46, v198
	v_mov_b32_e32 v47, v199
	s_ashr_i32 s3, s10, 12
	s_mul_hi_i32 s8, s3, 0xc000
	s_mul_i32 s3, s3, 0xc000
	s_add_u32 s3, s36, s3
	s_addc_u32 s9, s37, s8
	s_add_u32 s8, s3, 0x146000
	s_addc_u32 s9, s9, 0
	s_add_i32 s10, s10, s0
	s_add_i32 s2, s2, s13
	s_ashr_i32 s3, s2, 31
	s_lshl_b64 s[14:15], s[2:3], 2
	s_add_u32 s14, s11, s14
	s_addc_u32 s15, s12, s15
	s_cmpk_lt_i32 s10, 0x4000
	v_lshlrev_b32_e32 v0, 2, v16
	v_lshlrev_b32_e32 v1, 2, v18
	v_add_u32_e32 v0, s1, v0
	v_add_u32_e32 v1, s1, v1
	ds_read_b32 v16, v0 offset:32
	ds_read_b32 v18, v1 offset:32
	global_load_dwordx2 v[48:49], v[34:35], off offset:-2048
	global_load_dwordx2 v[50:51], v[34:35], off offset:-1536
	global_load_dwordx2 v[52:53], v[34:35], off offset:-1024
	global_load_dwordx4 v[0:3], v28, s[8:9]
	global_load_dwordx2 v[54:55], v[34:35], off offset:-512
	global_load_dwordx4 v[8:11], v64, s[8:9]
	global_load_dwordx4 v[4:7], v65, s[8:9]
	global_load_dwordx4 v[12:15], v66, s[8:9]
	global_load_dwordx2 v[56:57], v[34:35], off
	global_load_dwordx4 v[20:23], v36, s[8:9]
	global_load_dwordx4 v[24:27], v38, s[8:9]
	global_load_dwordx2 v[76:77], v[34:35], off offset:512
	global_load_dwordx2 v[78:79], v[34:35], off offset:1024
	global_load_dwordx2 v[80:81], v[34:35], off offset:1536
	global_load_dwordx4 v[68:71], v40, s[8:9]
	global_load_dwordx4 v[72:75], v42, s[8:9]
	v_lshl_add_u64 v[34:35], v[34:35], 0, s[6:7]
	s_waitcnt lgkmcnt(0)
; __device__ __forceinline__ float bf_lo(unsigned w) { return __uint_as_float(w << 16); }
; __device__ __forceinline__ float bf_hi(unsigned w) { return __uint_as_float(w & 0xffff0000u); }
; __device__ __forceinline__ f32x4 ld4_bf(const bf16_t* p) { const u32x2 w = *(const u32x2*)p; return (f32x4){bf_lo(w.x), bf_hi(w.x), bf_lo(w.y), bf_hi(w.y)}; }
; __device__ __forceinline__ float sq4(const f32x4 v) { return (v[0] * v[0] + v[1] * v[1]) + (v[2] * v[2] + v[3] * v[3]); }
; __device__ __forceinline__ void phase_final(const Ctx& P, volatile LAS int* tab, int vcu, int G) {
;     ...
;         const int e1 = tok[row * 8], pos1 = tok[row * 8 + 1], e2 = tok[row * 8 + 2], pos2 = tok[row * 8 + 3]; const float p1 = ((const float*)tok)[row * 8 + 4], p2 = ((const float*)tok)[row * 8 + 5];
;         const bf16_t* y1 = YB + (size_t)(tab[8 + e1] * 256 + pos1) * DM; const bf16_t* y2 = YB + (size_t)(tab[8 + e2] * 256 + pos2) * DM;
;         const bf16_t* xr = (const bf16_t*)(P.ws + WS_XA) + (size_t)row * DM; const float* g2 = mod + (size_t)(row >> 12) * NMOD + 5 * DM;
;         f32x4 v[8]; float ss = 0.f;
; #pragma unroll
;         for (int j = 0; j < 8; ++j) { const int c = 4 * lane + 256 * j; const f32x4 x4 = ld4_bf(xr + c), g4 = *(const f32x4*)(g2 + c); const u32x2 a = *(const u32x2*)(y1 + c), b = *(const u32x2*)(y2 + c);
;             const f32x4 ya = (f32x4){bf_lo(a.x), bf_hi(a.x), bf_lo(a.y), bf_hi(a.y)}, yb = (f32x4){bf_lo(b.x), bf_hi(b.x), bf_lo(b.y), bf_hi(b.y)};
;             v[j] = x4 + g4 * (ya * p1 + yb * p2); ss += sq4(v[j]); }
	v_lshlrev_b32_e32 v16, 8, v16
	v_lshlrev_b32_e32 v18, 8, v18
	v_add_u32_e32 v16, v16, v17
	v_add_u32_e32 v18, v18, v19
	v_ashrrev_i32_e32 v17, 31, v16
	v_ashrrev_i32_e32 v19, 31, v18
	v_lshlrev_b64 v[16:17], 12, v[16:17]
	v_lshlrev_b64 v[18:19], 12, v[18:19]
	v_lshl_add_u64 v[16:17], v[30:31], 0, v[16:17]
	v_lshl_add_u64 v[18:19], v[30:31], 0, v[18:19]
	global_load_dwordx2 v[84:85], v[16:17], off
	global_load_dwordx2 v[86:87], v[18:19], off
	global_load_dwordx2 v[88:89], v[16:17], off offset:512
	global_load_dwordx2 v[90:91], v[18:19], off offset:512
	global_load_dwordx2 v[92:93], v[16:17], off offset:1024
	global_load_dwordx2 v[94:95], v[18:19], off offset:1024
	global_load_dwordx2 v[96:97], v[16:17], off offset:1536
	global_load_dwordx2 v[98:99], v[18:19], off offset:1536
	global_load_dwordx2 v[100:101], v[16:17], off offset:2048
	global_load_dwordx2 v[102:103], v[18:19], off offset:2048
	global_load_dwordx2 v[104:105], v[16:17], off offset:2560
	global_load_dwordx2 v[106:107], v[16:17], off offset:3072
	global_load_dwordx2 v[108:109], v[16:17], off offset:3584
	global_load_dwordx2 v[110:111], v[18:19], off offset:2560
	global_load_dwordx2 v[112:113], v[18:19], off offset:3072
	global_load_dwordx2 v[114:115], v[18:19], off offset:3584
	global_load_dwordx4 v[194:197], v29, s[14:15]
	global_load_dwordx2 v[198:199], v29, s[14:15] offset:16
	s_waitcnt vmcnt(2)
	v_lshlrev_b32_e32 v116, 16, v48
	v_and_b32_e32 v117, 0xffff0000, v48
	v_lshlrev_b32_e32 v48, 16, v49
	v_and_b32_e32 v49, 0xffff0000, v49
	v_lshlrev_b32_e32 v118, 16, v50
	v_and_b32_e32 v119, 0xffff0000, v50
	v_lshlrev_b32_e32 v50, 16, v51
	v_and_b32_e32 v51, 0xffff0000, v51
	v_lshlrev_b32_e32 v120, 16, v52
	v_and_b32_e32 v121, 0xffff0000, v52
	v_lshlrev_b32_e32 v52, 16, v53
	v_and_b32_e32 v53, 0xffff0000, v53
	v_lshlrev_b32_e32 v124, 16, v56
	v_and_b32_e32 v125, 0xffff0000, v56
	v_lshlrev_b32_e32 v132, 16, v86
	v_and_b32_e32 v133, 0xffff0000, v86
	v_lshlrev_b32_e32 v86, 16, v87
	v_and_b32_e32 v87, 0xffff0000, v87
	v_lshlrev_b32_e32 v136, 16, v90
	v_and_b32_e32 v137, 0xffff0000, v90
	v_lshlrev_b32_e32 v90, 16, v91
	v_and_b32_e32 v91, 0xffff0000, v91
	v_lshlrev_b32_e32 v82, 16, v84
	v_and_b32_e32 v83, 0xffff0000, v84
	v_lshlrev_b32_e32 v84, 16, v85
	v_and_b32_e32 v85, 0xffff0000, v85
	v_lshlrev_b32_e32 v134, 16, v88
	v_and_b32_e32 v135, 0xffff0000, v88
	v_lshlrev_b32_e32 v88, 16, v89
	v_and_b32_e32 v89, 0xffff0000, v89
	v_lshlrev_b32_e32 v140, 16, v94
	v_and_b32_e32 v141, 0xffff0000, v94
	v_lshlrev_b32_e32 v94, 16, v95
	v_and_b32_e32 v95, 0xffff0000, v95
	v_lshlrev_b32_e32 v148, 16, v102
	v_and_b32_e32 v149, 0xffff0000, v102
	v_lshlrev_b32_e32 v102, 16, v103
	v_and_b32_e32 v103, 0xffff0000, v103
	v_lshlrev_b32_e32 v156, 16, v112
	v_and_b32_e32 v157, 0xffff0000, v112
	v_lshlrev_b32_e32 v112, 16, v113
	v_and_b32_e32 v113, 0xffff0000, v113
	v_pk_mul_f32 v[86:87], v[46:47], v[86:87] op_sel:[1,0]
	v_pk_mul_f32 v[132:133], v[46:47], v[132:133] op_sel:[1,0]
	v_pk_mul_f32 v[90:91], v[46:47], v[90:91] op_sel:[1,0]
	v_pk_mul_f32 v[136:137], v[46:47], v[136:137] op_sel:[1,0]
	v_lshlrev_b32_e32 v138, 16, v92
	v_and_b32_e32 v139, 0xffff0000, v92
	v_lshlrev_b32_e32 v92, 16, v93
	v_and_b32_e32 v93, 0xffff0000, v93
	v_lshlrev_b32_e32 v144, 16, v98
	v_and_b32_e32 v145, 0xffff0000, v98
	v_lshlrev_b32_e32 v98, 16, v99
	v_and_b32_e32 v99, 0xffff0000, v99
	v_lshlrev_b32_e32 v146, 16, v100
	v_and_b32_e32 v147, 0xffff0000, v100
	v_lshlrev_b32_e32 v100, 16, v101
	v_and_b32_e32 v101, 0xffff0000, v101
	v_lshlrev_b32_e32 v152, 16, v110
	v_and_b32_e32 v153, 0xffff0000, v110
	v_lshlrev_b32_e32 v110, 16, v111
	v_and_b32_e32 v111, 0xffff0000, v111
	v_lshlrev_b32_e32 v154, 16, v106
	v_and_b32_e32 v155, 0xffff0000, v106
	v_lshlrev_b32_e32 v106, 16, v107
	v_and_b32_e32 v107, 0xffff0000, v107
	v_lshlrev_b32_e32 v160, 16, v114
	v_and_b32_e32 v161, 0xffff0000, v114
	v_lshlrev_b32_e32 v114, 16, v115
	v_and_b32_e32 v115, 0xffff0000, v115
	v_pk_mul_f32 v[140:141], v[46:47], v[140:141] op_sel:[1,0]
	v_pk_mul_f32 v[94:95], v[46:47], v[94:95] op_sel:[1,0]
	v_pk_mul_f32 v[102:103], v[46:47], v[102:103] op_sel:[1,0]
	v_pk_mul_f32 v[112:113], v[46:47], v[112:113] op_sel:[1,0]
	v_pk_fma_f32 v[82:83], v[46:47], v[82:83], v[132:133] op_sel_hi:[0,1,1]
	v_pk_fma_f32 v[84:85], v[46:47], v[84:85], v[86:87] op_sel_hi:[0,1,1]
	v_pk_fma_f32 v[86:87], v[46:47], v[134:135], v[136:137] op_sel_hi:[0,1,1]
	v_pk_fma_f32 v[88:89], v[46:47], v[88:89], v[90:91] op_sel_hi:[0,1,1]
	v_lshlrev_b32_e32 v56, 16, v57
	v_and_b32_e32 v57, 0xffff0000, v57
	v_lshlrev_b32_e32 v128, 16, v78
	v_and_b32_e32 v129, 0xffff0000, v78
	v_lshlrev_b32_e32 v78, 16, v79
	v_and_b32_e32 v79, 0xffff0000, v79
	v_lshlrev_b32_e32 v142, 16, v96
	v_and_b32_e32 v143, 0xffff0000, v96
	v_lshlrev_b32_e32 v96, 16, v97
	v_and_b32_e32 v97, 0xffff0000, v97
	v_lshlrev_b32_e32 v150, 16, v104
	v_and_b32_e32 v151, 0xffff0000, v104
	v_lshlrev_b32_e32 v104, 16, v105
	v_and_b32_e32 v105, 0xffff0000, v105
	v_lshlrev_b32_e32 v158, 16, v108
	v_and_b32_e32 v159, 0xffff0000, v108
	v_lshlrev_b32_e32 v108, 16, v109
	v_and_b32_e32 v109, 0xffff0000, v109
	v_pk_mul_f32 v[98:99], v[46:47], v[98:99] op_sel:[1,0]
	v_pk_mul_f32 v[144:145], v[46:47], v[144:145] op_sel:[1,0]
	v_pk_mul_f32 v[148:149], v[46:47], v[148:149] op_sel:[1,0]
	v_pk_mul_f32 v[152:153], v[46:47], v[152:153] op_sel:[1,0]
	v_pk_mul_f32 v[110:111], v[46:47], v[110:111] op_sel:[1,0]
	v_pk_mul_f32 v[156:157], v[46:47], v[156:157] op_sel:[1,0]
	v_pk_mul_f32 v[114:115], v[46:47], v[114:115] op_sel:[1,0]
	v_pk_mul_f32 v[160:161], v[46:47], v[160:161] op_sel:[1,0]
	v_pk_fma_f32 v[90:91], v[46:47], v[92:93], v[94:95] op_sel_hi:[0,1,1]
; __device__ __forceinline__ float bf_lo(unsigned w) { return __uint_as_float(w << 16); }
; __device__ __forceinline__ float bf_hi(unsigned w) { return __uint_as_float(w & 0xffff0000u); }
; __device__ __forceinline__ f32x4 ld4_bf(const bf16_t* p) { const u32x2 w = *(const u32x2*)p; return (f32x4){bf_lo(w.x), bf_hi(w.x), bf_lo(w.y), bf_hi(w.y)}; }
; __device__ __forceinline__ float sq4(const f32x4 v) { return (v[0] * v[0] + v[1] * v[1]) + (v[2] * v[2] + v[3] * v[3]); }
; __device__ __forceinline__ void phase_final(const Ctx& P, volatile LAS int* tab, int vcu, int G) {
;     ...
;         for (int j = 0; j < 8; ++j) { const int c = 4 * lane + 256 * j; const f32x4 x4 = ld4_bf(xr + c), g4 = *(const f32x4*)(g2 + c); const u32x2 a = *(const u32x2*)(y1 + c), b = *(const u32x2*)(y2 + c);
;             const f32x4 ya = (f32x4){bf_lo(a.x), bf_hi(a.x), bf_lo(a.y), bf_hi(a.y)}, yb = (f32x4){bf_lo(b.x), bf_hi(b.x), bf_lo(b.y), bf_hi(b.y)};
;             v[j] = x4 + g4 * (ya * p1 + yb * p2); ss += sq4(v[j]); }
;         ss = wave_sum(ss); const float rstd = __builtin_amdgcn_rsqf(ss * (1.0f / DM) + EPS);
	v_pk_fma_f32 v[92:93], v[46:47], v[138:139], v[140:141] op_sel_hi:[0,1,1]
	v_pk_fma_f32 v[100:101], v[46:47], v[100:101], v[102:103] op_sel_hi:[0,1,1]
	v_pk_fma_f32 v[106:107], v[46:47], v[106:107], v[112:113] op_sel_hi:[0,1,1]
	v_pk_fma_f32 v[2:3], v[2:3], v[84:85], v[48:49]
	v_pk_fma_f32 v[0:1], v[0:1], v[82:83], v[116:117]
	v_pk_fma_f32 v[10:11], v[10:11], v[88:89], v[50:51]
	v_pk_fma_f32 v[8:9], v[8:9], v[86:87], v[118:119]
	v_lshlrev_b32_e32 v122, 16, v54
	v_and_b32_e32 v123, 0xffff0000, v54
	v_lshlrev_b32_e32 v54, 16, v55
	v_and_b32_e32 v55, 0xffff0000, v55
	v_lshlrev_b32_e32 v130, 16, v80
	v_and_b32_e32 v131, 0xffff0000, v80
	v_lshlrev_b32_e32 v80, 16, v81
	v_and_b32_e32 v81, 0xffff0000, v81
	v_pk_fma_f32 v[94:95], v[46:47], v[142:143], v[144:145] op_sel_hi:[0,1,1]
	v_pk_fma_f32 v[96:97], v[46:47], v[96:97], v[98:99] op_sel_hi:[0,1,1]
	v_pk_fma_f32 v[98:99], v[46:47], v[146:147], v[148:149] op_sel_hi:[0,1,1]
	v_pk_fma_f32 v[102:103], v[46:47], v[104:105], v[110:111] op_sel_hi:[0,1,1]
	v_pk_fma_f32 v[104:105], v[46:47], v[150:151], v[152:153] op_sel_hi:[0,1,1]
	v_pk_fma_f32 v[110:111], v[46:47], v[154:155], v[156:157] op_sel_hi:[0,1,1]
	v_pk_fma_f32 v[112:113], v[46:47], v[158:159], v[160:161] op_sel_hi:[0,1,1]
	v_pk_fma_f32 v[46:47], v[46:47], v[108:109], v[114:115] op_sel_hi:[0,1,1]
	v_pk_fma_f32 v[4:5], v[4:5], v[92:93], v[120:121]
	v_pk_fma_f32 v[6:7], v[6:7], v[90:91], v[52:53]
	v_pk_fma_f32 v[22:23], v[22:23], v[100:101], v[56:57]
	v_pk_fma_f32 v[48:49], v[70:71], v[106:107], v[78:79]
	v_mov_b32_e32 v56, v1
	v_mov_b32_e32 v57, v9
	v_mov_b32_e32 v70, v3
	v_mov_b32_e32 v71, v11
	v_pk_fma_f32 v[14:15], v[14:15], v[96:97], v[54:55]
	v_pk_fma_f32 v[50:51], v[68:69], v[110:111], v[128:129]
	v_pk_fma_f32 v[46:47], v[74:75], v[46:47], v[80:81]
	v_pk_fma_f32 v[52:53], v[72:73], v[112:113], v[130:131]
	v_mov_b32_e32 v54, v0
	v_mov_b32_e32 v55, v8
	v_mov_b32_e32 v68, v2
	v_mov_b32_e32 v69, v10
	v_pk_mul_f32 v[72:73], v[6:7], v[6:7]
	v_pk_mul_f32 v[74:75], v[4:5], v[4:5]
	v_pk_mul_f32 v[56:57], v[56:57], v[56:57]
	v_pk_mul_f32 v[70:71], v[70:71], v[70:71]
	v_lshlrev_b32_e32 v126, 16, v76
	v_and_b32_e32 v127, 0xffff0000, v76
	v_lshlrev_b32_e32 v76, 16, v77
	v_and_b32_e32 v77, 0xffff0000, v77
	v_pk_fma_f32 v[12:13], v[12:13], v[94:95], v[122:123]
	v_pk_mov_b32 v[88:89], v[74:75], v[72:73] op_sel:[1,0]
	v_mov_b32_e32 v75, v73
	v_pk_fma_f32 v[54:55], v[54:55], v[54:55], v[56:57]
	v_pk_fma_f32 v[56:57], v[68:69], v[68:69], v[70:71]
	v_pk_fma_f32 v[20:21], v[20:21], v[98:99], v[124:125]
	v_pk_fma_f32 v[26:27], v[26:27], v[102:103], v[76:77]
	v_mul_f32_e32 v76, v13, v13
	v_mul_f32_e32 v78, v15, v15
	v_pk_add_f32 v[68:69], v[88:89], v[74:75]
	v_pk_add_f32 v[54:55], v[54:55], v[56:57]
	v_pk_fma_f32 v[24:25], v[24:25], v[104:105], v[126:127]
	v_mul_f32_e32 v87, v20, v20
	v_mul_f32_e32 v90, v21, v21
	v_mul_f32_e32 v91, v22, v22
	v_mul_f32_e32 v92, v23, v23
	v_pk_fma_f32 v[72:73], v[12:13], v[12:13], v[76:77] op_sel_hi:[1,1,0]
	v_pk_fma_f32 v[76:77], v[14:15], v[14:15], v[78:79] op_sel_hi:[1,1,0]
	v_pk_add_f32 v[56:57], v[68:69], v[68:69] op_sel:[0,1] op_sel_hi:[1,0]
	v_pk_add_f32 v[54:55], v[54:55], v[54:55] op_sel:[0,1] op_sel_hi:[1,0]
	v_pk_mul_f32 v[80:81], v[26:27], v[26:27]
	v_pk_mul_f32 v[82:83], v[24:25], v[24:25]
	v_mov_b32_e32 v73, v91
	v_mov_b32_e32 v77, v92
	v_mov_b32_e32 v57, v90
	v_mov_b32_e32 v55, v87
	v_pk_mov_b32 v[78:79], v[82:83], v[80:81] op_sel:[1,0]
	v_mov_b32_e32 v83, v81
	v_pk_add_f32 v[68:69], v[72:73], v[76:77]
	v_pk_add_f32 v[54:55], v[54:55], v[56:57]
	v_mul_f32_e32 v84, v51, v51
	v_mul_f32_e32 v86, v49, v49
	v_pk_add_f32 v[70:71], v[78:79], v[82:83]
	v_pk_add_f32 v[54:55], v[54:55], v[68:69]
	v_mul_f32_e32 v93, v52, v52
	v_mul_f32_e32 v94, v53, v53
	v_mul_f32_e32 v95, v46, v46
	v_mul_f32_e32 v96, v47, v47
	v_pk_fma_f32 v[80:81], v[50:51], v[50:51], v[84:85] op_sel_hi:[1,1,0]
	v_pk_fma_f32 v[84:85], v[48:49], v[48:49], v[86:87] op_sel_hi:[1,1,0]
	v_pk_add_f32 v[70:71], v[70:71], v[70:71] op_sel:[0,1] op_sel_hi:[1,0]
	v_pk_add_f32 v[54:55], v[54:55], v[54:55] op_sel:[0,1] op_sel_hi:[1,0]
	v_mov_b32_e32 v81, v95
	v_mov_b32_e32 v85, v96
	v_mov_b32_e32 v71, v94
	v_mov_b32_e32 v55, v93
	v_pk_add_f32 v[72:73], v[80:81], v[84:85]
	v_pk_add_f32 v[54:55], v[54:55], v[70:71]
	s_nop 0
	v_pk_add_f32 v[54:55], v[54:55], v[72:73]
	s_nop 0
	v_add_f32_e32 v54, v54, v55
	ds_bpermute_b32 v55, v58, v54
	s_waitcnt lgkmcnt(0)
; __device__ __forceinline__ void phase_final(const Ctx& P, volatile LAS int* tab, int vcu, int G) {
;     ...
;         ss = wave_sum(ss); const float rstd = __builtin_amdgcn_rsqf(ss * (1.0f / DM) + EPS);
; #pragma unroll
;         for (int j = 0; j < 8; ++j) { const int c = 4 * lane + 256 * j; const f32x4 fg = *(const f32x4*)(P.in[34] + c); *(f32x4*)(P.out + (size_t)row * DM + c) = v[j] * rstd * fg; }
	v_add_f32_e32 v54, v54, v55
	ds_bpermute_b32 v55, v59, v54
	s_waitcnt lgkmcnt(0)
	v_add_f32_e32 v54, v54, v55
	ds_bpermute_b32 v55, v60, v54
	s_waitcnt lgkmcnt(0)
	v_add_f32_e32 v54, v54, v55
	ds_bpermute_b32 v55, v61, v54
	s_waitcnt lgkmcnt(0)
	v_add_f32_e32 v54, v54, v55
	ds_bpermute_b32 v55, v62, v54
	s_waitcnt lgkmcnt(0)
	v_add_f32_e32 v54, v54, v55
	ds_bpermute_b32 v55, v63, v54
	s_waitcnt lgkmcnt(0)
	v_add_f32_e32 v54, v54, v55
	v_fmamk_f32 v54, v54, 0x3a000000, v67
	v_rsq_f32_e32 v54, v54
	s_nop 0
	v_pk_mul_f32 v[0:1], v[0:1], v[54:55] op_sel_hi:[1,0]
	v_pk_mul_f32 v[2:3], v[2:3], v[54:55] op_sel_hi:[1,0]
	v_pk_mul_f32 v[8:9], v[8:9], v[54:55] op_sel_hi:[1,0]
	v_pk_mul_f32 v[10:11], v[10:11], v[54:55] op_sel_hi:[1,0]
	v_pk_mul_f32 v[4:5], v[4:5], v[54:55] op_sel_hi:[1,0]
	v_pk_mul_f32 v[6:7], v[6:7], v[54:55] op_sel_hi:[1,0]
	v_pk_mul_f32 v[12:13], v[12:13], v[54:55] op_sel_hi:[1,0]
	v_pk_mul_f32 v[14:15], v[14:15], v[54:55] op_sel_hi:[1,0]
	v_pk_mul_f32 v[20:21], v[20:21], v[54:55] op_sel_hi:[1,0]
	v_pk_mul_f32 v[22:23], v[22:23], v[54:55] op_sel_hi:[1,0]
	v_pk_mul_f32 v[24:25], v[24:25], v[54:55] op_sel_hi:[1,0]
	v_pk_mul_f32 v[26:27], v[26:27], v[54:55] op_sel_hi:[1,0]
	v_pk_mul_f32 v[68:69], v[50:51], v[54:55] op_sel_hi:[1,0]
	v_pk_mul_f32 v[70:71], v[48:49], v[54:55] op_sel_hi:[1,0]
	v_pk_mul_f32 v[72:73], v[52:53], v[54:55] op_sel_hi:[1,0]
	v_pk_mul_f32 v[74:75], v[46:47], v[54:55] op_sel_hi:[1,0]
	v_pk_mul_f32 v[0:1], v[162:163], v[0:1]
	v_pk_mul_f32 v[2:3], v[164:165], v[2:3]
	global_store_dwordx4 v[32:33], v[0:3], off offset:-4096
	v_pk_mul_f32 v[8:9], v[166:167], v[8:9]
	v_pk_mul_f32 v[10:11], v[168:169], v[10:11]
	global_store_dwordx4 v[32:33], v[8:11], off offset:-3072
	v_pk_mul_f32 v[4:5], v[170:171], v[4:5]
	v_pk_mul_f32 v[6:7], v[172:173], v[6:7]
	global_store_dwordx4 v[32:33], v[4:7], off offset:-2048
	v_pk_mul_f32 v[12:13], v[174:175], v[12:13]
	v_pk_mul_f32 v[14:15], v[176:177], v[14:15]
	global_store_dwordx4 v[32:33], v[12:15], off offset:-1024
	v_pk_mul_f32 v[20:21], v[178:179], v[20:21]
	v_pk_mul_f32 v[22:23], v[180:181], v[22:23]
	global_store_dwordx4 v[32:33], v[20:23], off
	v_pk_mul_f32 v[24:25], v[182:183], v[24:25]
	v_pk_mul_f32 v[26:27], v[184:185], v[26:27]
	global_store_dwordx4 v[32:33], v[24:27], off offset:1024
	v_pk_mul_f32 v[68:69], v[186:187], v[68:69]
	v_pk_mul_f32 v[70:71], v[188:189], v[70:71]
	global_store_dwordx4 v[32:33], v[68:71], off offset:2048
	v_pk_mul_f32 v[72:73], v[190:191], v[72:73]
	v_pk_mul_f32 v[74:75], v[192:193], v[74:75]
	global_store_dwordx4 v[32:33], v[72:75], off offset:3072
	v_lshl_add_u64 v[32:33], v[32:33], 0, s[4:5]
	s_waitcnt vmcnt(8)
	s_cbranch_scc1 .LBB0_2712
